# v16: + exact counted waits for the first two side-job visits of a phase (k=2 case) (m1)
# speedup vs baseline: 1.0137x; 1.0081x over previous
.Lp1vg_mmafter_b:
	s_barrier
	s_mov_b32 m0, s69
	v_lshl_add_u64 v[4:5], v[4:5], 0, s[24:25]
	s_add_u32 s4, s56, 0x80080
	ds_read_b128 v[174:177], v234 offset:49152
	ds_read_b128 v[178:181], v234 offset:50176
	ds_read_b128 v[182:185], v234 offset:51200
	ds_read_b128 v[186:189], v234 offset:52224
	ds_read_b128 v[190:193], v234 offset:53248
	ds_read_b128 v[194:197], v234 offset:54272
	ds_read_b128 v[198:201], v234 offset:55296
	ds_read_b128 v[202:205], v234 offset:56320
	global_load_lds_dwordx4 v[4:5], off
	v_lshl_add_u64 v[4:5], v[226:227], 0, s[24:25]
	s_mov_b32 m0, s70
	s_addc_u32 s5, s57, 0
	global_load_lds_dwordx4 v[4:5], off
	v_lshl_add_u64 v[4:5], s[4:5], 0, v[212:213]
	s_mov_b32 m0, s73
	s_nop 0
	global_load_lds_dwordx4 v[4:5], off
	v_lshl_add_u64 v[4:5], s[4:5], 0, v[216:217]
	s_mov_b32 m0, s75
	s_nop 0
	global_load_lds_dwordx4 v[4:5], off
	v_lshl_add_u64 v[4:5], v[228:229], 0, s[24:25]
	s_mov_b32 m0, s71
	s_nop 0
	global_load_lds_dwordx4 v[4:5], off
	v_lshl_add_u64 v[4:5], v[230:231], 0, s[24:25]
	s_mov_b32 m0, s72
	s_nop 0
	global_load_lds_dwordx4 v[4:5], off
	s_cmp_eq_u32 s100, 3
	s_cbranch_scc1 .Lp1vg_w11_b2
	s_cmp_eq_u32 s100, 2
	s_cbranch_scc1 .Lp1vg_wk2_b2
	s_waitcnt vmcnt(8)
	s_branch .Lp1vg_wd_b2
.Lp1vg_wk2_b2:
	s_waitcnt vmcnt(10)
	s_branch .Lp1vg_wd_b2

.LBB0_168:
	ds_read_b128 v[158:161], v232
	ds_read_b128 v[162:165], v232 offset:1024
	ds_read_b128 v[166:169], v232 offset:2048
	ds_read_b128 v[170:173], v232 offset:3072
	ds_read_b128 v[142:145], v233
	ds_read_b128 v[146:149], v233 offset:1024
	ds_read_b128 v[150:153], v233 offset:2048
	ds_read_b128 v[154:157], v233 offset:3072
	v_lshl_add_u64 v[4:5], s[54:55], 0, v[218:219]
	s_add_i32 m0, s41, 0xc000
	ds_read_b128 v[198:201], v234
	ds_read_b128 v[202:205], v234 offset:1024
	ds_read_b128 v[190:193], v234 offset:2048
	ds_read_b128 v[194:197], v234 offset:3072
	ds_read_b128 v[182:185], v234 offset:4096
	ds_read_b128 v[186:189], v234 offset:5120
	ds_read_b128 v[174:177], v234 offset:6144
	ds_read_b128 v[178:181], v234 offset:7168
	global_load_lds_dwordx4 v[4:5], off
	v_lshl_add_u64 v[4:5], s[54:55], 0, v[220:221]
	s_add_i32 m0, s41, 0xe000
	s_nop 0
	global_load_lds_dwordx4 v[4:5], off
	s_cmp_eq_u32 s100, 3
	s_cbranch_scc1 .Lp1vg_w11_a1
	s_cmp_eq_u32 s100, 2
	s_cbranch_scc1 .Lp1vg_wk2_a1
	s_waitcnt vmcnt(8)
	s_branch .Lp1vg_wd_a1

.Lp1vg_mmjoin_a:
	s_barrier
	s_mov_b32 m0, s53
	v_lshl_add_u64 v[4:5], s[56:57], 0, v[212:213]
	s_add_u32 s82, s56, 0x80000
	ds_read_b128 v[174:177], v234 offset:16384
	ds_read_b128 v[178:181], v234 offset:17408
	ds_read_b128 v[182:185], v234 offset:18432
	ds_read_b128 v[186:189], v234 offset:19456
	ds_read_b128 v[190:193], v234 offset:20480
	ds_read_b128 v[194:197], v234 offset:21504
	ds_read_b128 v[198:201], v234 offset:22528
	ds_read_b128 v[202:205], v234 offset:23552
	global_load_lds_dwordx4 v[4:5], off
	v_lshl_add_u64 v[226:227], s[56:57], 0, v[216:217]
	s_mov_b32 m0, s60
	s_addc_u32 s83, s57, 0
	global_load_lds_dwordx4 v[226:227], off
	v_lshl_add_u64 v[228:229], s[82:83], 0, v[212:213]
	s_mov_b32 m0, s61
	v_lshl_add_u64 v[230:231], s[4:5], 0, v[214:215]
	global_load_lds_dwordx4 v[228:229], off
	v_lshl_add_u64 v[228:229], s[82:83], 0, v[216:217]
	s_mov_b32 m0, s64
	s_nop 0
	global_load_lds_dwordx4 v[228:229], off
	v_lshl_add_u64 v[228:229], s[4:5], 0, v[210:211]
	s_mov_b32 m0, s41
	s_nop 0
	global_load_lds_dwordx4 v[228:229], off
	s_mov_b32 m0, s65
	s_nop 0
	global_load_lds_dwordx4 v[230:231], off
	s_cmp_eq_u32 s100, 3
	s_cbranch_scc1 .Lp1vg_w11_a2
	s_cmp_eq_u32 s100, 2
	s_cbranch_scc1 .Lp1vg_wk2_a2
	s_waitcnt vmcnt(8)
	s_branch .Lp1vg_wd_a2

.Lp1vg_wd_a2:
	s_waitcnt lgkmcnt(0)
	s_barrier
	s_setprio 1
	s_waitcnt lgkmcnt(0)
	v_mfma_f32_16x16x32_bf16 v[74:77], v[158:161], v[174:177], v[74:77]
	v_mfma_f32_16x16x32_bf16 v[70:73], v[166:169], v[174:177], v[70:73]
	v_mfma_f32_16x16x32_bf16 v[58:61], v[158:161], v[182:185], v[58:61]
	v_mfma_f32_16x16x32_bf16 v[54:57], v[166:169], v[182:185], v[54:57]
	v_mfma_f32_16x16x32_bf16 v[42:45], v[158:161], v[190:193], v[42:45]
	v_mfma_f32_16x16x32_bf16 v[38:41], v[166:169], v[190:193], v[38:41]
	v_mfma_f32_16x16x32_bf16 v[26:29], v[158:161], v[198:201], v[26:29]
	v_mfma_f32_16x16x32_bf16 v[22:25], v[166:169], v[198:201], v[22:25]
	v_mfma_f32_16x16x32_bf16 v[74:77], v[162:165], v[178:181], v[74:77]
	v_mfma_f32_16x16x32_bf16 v[70:73], v[170:173], v[178:181], v[70:73]
	v_mfma_f32_16x16x32_bf16 v[58:61], v[162:165], v[186:189], v[58:61]
	v_mfma_f32_16x16x32_bf16 v[54:57], v[170:173], v[186:189], v[54:57]
	v_mfma_f32_16x16x32_bf16 v[42:45], v[162:165], v[194:197], v[42:45]
	v_mfma_f32_16x16x32_bf16 v[38:41], v[170:173], v[194:197], v[38:41]
	v_mfma_f32_16x16x32_bf16 v[26:29], v[162:165], v[202:205], v[26:29]
	v_mfma_f32_16x16x32_bf16 v[22:25], v[170:173], v[202:205], v[22:25]
	s_setprio 0
	s_setprio 1
	v_mfma_f32_16x16x32_bf16 v[66:69], v[142:145], v[174:177], v[66:69]
	v_mfma_f32_16x16x32_bf16 v[62:65], v[150:153], v[174:177], v[62:65]
	v_mfma_f32_16x16x32_bf16 v[50:53], v[142:145], v[182:185], v[50:53]
	v_mfma_f32_16x16x32_bf16 v[46:49], v[150:153], v[182:185], v[46:49]
	v_mfma_f32_16x16x32_bf16 v[34:37], v[142:145], v[190:193], v[34:37]
	v_mfma_f32_16x16x32_bf16 v[30:33], v[150:153], v[190:193], v[30:33]
	v_mfma_f32_16x16x32_bf16 v[18:21], v[142:145], v[198:201], v[18:21]
	v_mfma_f32_16x16x32_bf16 v[14:17], v[150:153], v[198:201], v[14:17]
	v_mfma_f32_16x16x32_bf16 v[66:69], v[146:149], v[178:181], v[66:69]
	v_mfma_f32_16x16x32_bf16 v[62:65], v[154:157], v[178:181], v[62:65]
	v_mfma_f32_16x16x32_bf16 v[50:53], v[146:149], v[186:189], v[50:53]
	v_mfma_f32_16x16x32_bf16 v[46:49], v[154:157], v[186:189], v[46:49]
	v_mfma_f32_16x16x32_bf16 v[34:37], v[146:149], v[194:197], v[34:37]
	v_mfma_f32_16x16x32_bf16 v[30:33], v[154:157], v[194:197], v[30:33]
	v_mfma_f32_16x16x32_bf16 v[18:21], v[146:149], v[202:205], v[18:21]
	v_mfma_f32_16x16x32_bf16 v[14:17], v[154:157], v[202:205], v[14:17]
	s_setprio 0
	s_barrier
	v_add_u32_e32 v2, 0x18000, v209
	ds_read_b128 v[158:161], v2
	ds_read_b128 v[162:165], v2 offset:1024
	ds_read_b128 v[166:169], v2 offset:2048
	ds_read_b128 v[170:173], v2 offset:3072
	v_add_u32_e32 v2, 0x1c000, v209
	ds_read_b128 v[142:145], v2
	ds_read_b128 v[146:149], v2 offset:1024
	ds_read_b128 v[150:153], v2 offset:2048
	ds_read_b128 v[154:157], v2 offset:3072
	s_add_u32 s4, s4, 0x80000
	s_addc_u32 s5, s5, 0
	s_mov_b32 m0, s66
	v_lshl_add_u64 v[238:239], s[4:5], 0, v[210:211]
	ds_read_b128 v[198:201], v234 offset:32768
	ds_read_b128 v[202:205], v234 offset:33792
	ds_read_b128 v[190:193], v234 offset:34816
	ds_read_b128 v[194:197], v234 offset:35840
	ds_read_b128 v[182:185], v234 offset:36864
	ds_read_b128 v[186:189], v234 offset:37888
	ds_read_b128 v[174:177], v234 offset:38912
	ds_read_b128 v[178:181], v234 offset:39936
	global_load_lds_dwordx4 v[238:239], off
	v_lshl_add_u64 v[238:239], s[4:5], 0, v[214:215]
	s_mov_b32 m0, s67
	s_nop 0
	global_load_lds_dwordx4 v[238:239], off
	s_cmp_eq_u32 s100, 3
	s_cbranch_scc1 .Lp1vg_w11_b1
	s_cmp_eq_u32 s100, 2
	s_cbranch_scc1 .Lp1vg_wk2_b1
	s_waitcnt vmcnt(8)
	s_branch .Lp1vg_wd_b1

.Lp4vg_mmafter_b:
	s_barrier
	s_mov_b32 m0, s48
	v_lshl_add_u64 v[4:5], v[4:5], 0, s[0:1]
	s_add_u32 s4, s34, 0x80080
	ds_read_b128 v[174:177], v230 offset:49152
	ds_read_b128 v[178:181], v230 offset:50176
	ds_read_b128 v[182:185], v230 offset:51200
	ds_read_b128 v[186:189], v230 offset:52224
	ds_read_b128 v[190:193], v230 offset:53248
	ds_read_b128 v[194:197], v230 offset:54272
	ds_read_b128 v[198:201], v230 offset:55296
	ds_read_b128 v[202:205], v230 offset:56320
	global_load_lds_dwordx4 v[4:5], off
	v_lshl_add_u64 v[4:5], v[222:223], 0, s[0:1]
	s_mov_b32 m0, s49
	s_addc_u32 s5, s35, 0
	global_load_lds_dwordx4 v[4:5], off
	v_lshl_add_u64 v[4:5], s[4:5], 0, v[210:211]
	s_mov_b32 m0, s52
	s_nop 0
	global_load_lds_dwordx4 v[4:5], off
	v_lshl_add_u64 v[4:5], s[4:5], 0, v[212:213]
	s_mov_b32 m0, s53
	s_nop 0
	global_load_lds_dwordx4 v[4:5], off
	v_lshl_add_u64 v[4:5], v[224:225], 0, s[0:1]
	s_mov_b32 m0, s50
	s_nop 0
	global_load_lds_dwordx4 v[4:5], off
	v_lshl_add_u64 v[4:5], v[226:227], 0, s[0:1]
	s_mov_b32 m0, s51
	s_nop 0
	global_load_lds_dwordx4 v[4:5], off
	s_cmp_eq_u32 s100, 3
	s_cbranch_scc1 .Lp4vg_w11_b2
	s_cmp_eq_u32 s100, 2
	s_cbranch_scc1 .Lp4vg_wk2_b2
	s_waitcnt vmcnt(8)
	s_branch .Lp4vg_wd_b2

.LBB0_536:
	ds_read_b128 v[158:161], v228
	ds_read_b128 v[162:165], v228 offset:1024
	ds_read_b128 v[166:169], v228 offset:2048
	ds_read_b128 v[170:173], v228 offset:3072
	ds_read_b128 v[142:145], v229
	ds_read_b128 v[146:149], v229 offset:1024
	ds_read_b128 v[150:153], v229 offset:2048
	ds_read_b128 v[154:157], v229 offset:3072
	v_lshl_add_u64 v[4:5], s[24:25], 0, v[214:215]
	s_add_i32 m0, s21, 0xc000
	ds_read_b128 v[198:201], v230
	ds_read_b128 v[202:205], v230 offset:1024
	ds_read_b128 v[190:193], v230 offset:2048
	ds_read_b128 v[194:197], v230 offset:3072
	ds_read_b128 v[182:185], v230 offset:4096
	ds_read_b128 v[186:189], v230 offset:5120
	ds_read_b128 v[174:177], v230 offset:6144
	ds_read_b128 v[178:181], v230 offset:7168
	global_load_lds_dwordx4 v[4:5], off
	v_lshl_add_u64 v[4:5], s[24:25], 0, v[216:217]
	s_add_i32 m0, s21, 0xe000
	s_nop 0
	global_load_lds_dwordx4 v[4:5], off
	s_cmp_eq_u32 s100, 3
	s_cbranch_scc1 .Lp4vg_w11_a1
	s_cmp_eq_u32 s100, 2
	s_cbranch_scc1 .Lp4vg_wk2_a1
	s_waitcnt vmcnt(8)
	s_branch .Lp4vg_wd_a1

.Lp4vg_mmjoin_a:
	s_barrier
	s_mov_b32 m0, s33
	v_lshl_add_u64 v[4:5], s[34:35], 0, v[210:211]
	s_add_u32 s64, s34, 0x80000
	ds_read_b128 v[174:177], v230 offset:16384
	ds_read_b128 v[178:181], v230 offset:17408
	ds_read_b128 v[182:185], v230 offset:18432
	ds_read_b128 v[186:189], v230 offset:19456
	ds_read_b128 v[190:193], v230 offset:20480
	ds_read_b128 v[194:197], v230 offset:21504
	ds_read_b128 v[198:201], v230 offset:22528
	ds_read_b128 v[202:205], v230 offset:23552
	global_load_lds_dwordx4 v[4:5], off
	v_lshl_add_u64 v[222:223], s[34:35], 0, v[212:213]
	s_mov_b32 m0, s36
	s_addc_u32 s65, s35, 0
	global_load_lds_dwordx4 v[222:223], off
	v_lshl_add_u64 v[224:225], s[64:65], 0, v[210:211]
	s_mov_b32 m0, s37
	v_lshl_add_u64 v[226:227], s[4:5], 0, v[212:213]
	global_load_lds_dwordx4 v[224:225], off
	v_lshl_add_u64 v[224:225], s[64:65], 0, v[212:213]
	s_mov_b32 m0, s41
	s_nop 0
	global_load_lds_dwordx4 v[224:225], off
	v_lshl_add_u64 v[224:225], s[4:5], 0, v[210:211]
	s_mov_b32 m0, s21
	s_nop 0
	global_load_lds_dwordx4 v[224:225], off
	s_mov_b32 m0, s43
	s_nop 0
	global_load_lds_dwordx4 v[226:227], off
	s_cmp_eq_u32 s100, 3
	s_cbranch_scc1 .Lp4vg_w11_a2
	s_cmp_eq_u32 s100, 2
	s_cbranch_scc1 .Lp4vg_wk2_a2
	s_waitcnt vmcnt(8)
	s_branch .Lp4vg_wd_a2

.Lp4vg_wd_a2:
	s_waitcnt lgkmcnt(0)
	s_barrier
	s_setprio 1
	s_waitcnt lgkmcnt(0)
	v_mfma_f32_16x16x32_bf16 v[74:77], v[158:161], v[174:177], v[74:77]
	v_mfma_f32_16x16x32_bf16 v[70:73], v[166:169], v[174:177], v[70:73]
	v_mfma_f32_16x16x32_bf16 v[62:65], v[158:161], v[182:185], v[62:65]
	v_mfma_f32_16x16x32_bf16 v[58:61], v[166:169], v[182:185], v[58:61]
	v_mfma_f32_16x16x32_bf16 v[46:49], v[158:161], v[190:193], v[46:49]
	v_mfma_f32_16x16x32_bf16 v[42:45], v[166:169], v[190:193], v[42:45]
	v_mfma_f32_16x16x32_bf16 v[30:33], v[158:161], v[198:201], v[30:33]
	v_mfma_f32_16x16x32_bf16 v[26:29], v[166:169], v[198:201], v[26:29]
	v_mfma_f32_16x16x32_bf16 v[74:77], v[162:165], v[178:181], v[74:77]
	v_mfma_f32_16x16x32_bf16 v[70:73], v[170:173], v[178:181], v[70:73]
	v_mfma_f32_16x16x32_bf16 v[62:65], v[162:165], v[186:189], v[62:65]
	v_mfma_f32_16x16x32_bf16 v[58:61], v[170:173], v[186:189], v[58:61]
	v_mfma_f32_16x16x32_bf16 v[46:49], v[162:165], v[194:197], v[46:49]
	v_mfma_f32_16x16x32_bf16 v[42:45], v[170:173], v[194:197], v[42:45]
	v_mfma_f32_16x16x32_bf16 v[30:33], v[162:165], v[202:205], v[30:33]
	v_mfma_f32_16x16x32_bf16 v[26:29], v[170:173], v[202:205], v[26:29]
	s_setprio 0
	s_setprio 1
	v_mfma_f32_16x16x32_bf16 v[66:69], v[142:145], v[174:177], v[66:69]
	v_mfma_f32_16x16x32_bf16 v[54:57], v[150:153], v[174:177], v[54:57]
	v_mfma_f32_16x16x32_bf16 v[50:53], v[142:145], v[182:185], v[50:53]
	v_mfma_f32_16x16x32_bf16 v[38:41], v[150:153], v[182:185], v[38:41]
	v_mfma_f32_16x16x32_bf16 v[34:37], v[142:145], v[190:193], v[34:37]
	v_mfma_f32_16x16x32_bf16 v[22:25], v[150:153], v[190:193], v[22:25]
	v_mfma_f32_16x16x32_bf16 v[18:21], v[142:145], v[198:201], v[18:21]
	v_mfma_f32_16x16x32_bf16 v[14:17], v[150:153], v[198:201], v[14:17]
	v_mfma_f32_16x16x32_bf16 v[66:69], v[146:149], v[178:181], v[66:69]
	v_mfma_f32_16x16x32_bf16 v[54:57], v[154:157], v[178:181], v[54:57]
	v_mfma_f32_16x16x32_bf16 v[50:53], v[146:149], v[186:189], v[50:53]
	v_mfma_f32_16x16x32_bf16 v[38:41], v[154:157], v[186:189], v[38:41]
	v_mfma_f32_16x16x32_bf16 v[34:37], v[146:149], v[194:197], v[34:37]
	v_mfma_f32_16x16x32_bf16 v[22:25], v[154:157], v[194:197], v[22:25]
	v_mfma_f32_16x16x32_bf16 v[18:21], v[146:149], v[202:205], v[18:21]
	v_mfma_f32_16x16x32_bf16 v[14:17], v[154:157], v[202:205], v[14:17]
	s_setprio 0
	s_barrier
	v_add_u32_e32 v2, 0x18000, v1
	ds_read_b128 v[158:161], v2
	ds_read_b128 v[162:165], v2 offset:1024
	ds_read_b128 v[166:169], v2 offset:2048
	ds_read_b128 v[170:173], v2 offset:3072
	v_add_u32_e32 v2, 0x1c000, v1
	ds_read_b128 v[142:145], v2
	ds_read_b128 v[146:149], v2 offset:1024
	ds_read_b128 v[150:153], v2 offset:2048
	ds_read_b128 v[154:157], v2 offset:3072
	s_add_u32 s4, s4, 0x80000
	s_addc_u32 s5, s5, 0
	s_mov_b32 m0, s44
	v_lshl_add_u64 v[232:233], s[4:5], 0, v[210:211]
	ds_read_b128 v[198:201], v230 offset:32768
	ds_read_b128 v[202:205], v230 offset:33792
	ds_read_b128 v[190:193], v230 offset:34816
	ds_read_b128 v[194:197], v230 offset:35840
	ds_read_b128 v[182:185], v230 offset:36864
	ds_read_b128 v[186:189], v230 offset:37888
	ds_read_b128 v[174:177], v230 offset:38912
	ds_read_b128 v[178:181], v230 offset:39936
	global_load_lds_dwordx4 v[232:233], off
	v_lshl_add_u64 v[232:233], s[4:5], 0, v[212:213]
	s_mov_b32 m0, s46
	s_nop 0
	global_load_lds_dwordx4 v[232:233], off
	s_cmp_eq_u32 s100, 3
	s_cbranch_scc1 .Lp4vg_w11_b1
	s_cmp_eq_u32 s100, 2
	s_cbranch_scc1 .Lp4vg_wk2_b1
	s_waitcnt vmcnt(8)
	s_branch .Lp4vg_wd_b1

.LBB0_782:
	ds_read_b64_tr_b16 v[26:27], v228 offset:0
	ds_read_b64_tr_b16 v[28:29], v228 offset:1024
	ds_read_b64_tr_b16 v[30:31], v228 offset:8192
	ds_read_b64_tr_b16 v[32:33], v228 offset:9216
	ds_read_b64_tr_b16 v[18:19], v232 offset:0
	ds_read_b64_tr_b16 v[20:21], v232 offset:1024
	ds_read_b64_tr_b16 v[22:23], v232 offset:8192
	ds_read_b64_tr_b16 v[24:25], v232 offset:9216
	ds_read_b64_tr_b16 v[10:11], v229 offset:0
	ds_read_b64_tr_b16 v[12:13], v229 offset:1024
	ds_read_b64_tr_b16 v[14:15], v229 offset:8192
	ds_read_b64_tr_b16 v[16:17], v229 offset:9216
	ds_read_b64_tr_b16 v[2:3], v233 offset:0
	ds_read_b64_tr_b16 v[4:5], v233 offset:1024
	ds_read_b64_tr_b16 v[6:7], v233 offset:8192
	ds_read_b64_tr_b16 v[8:9], v233 offset:9216
	v_lshl_add_u64 v[68:69], s[42:43], 0, v[220:221]
	s_add_i32 m0, s15, 0xc000
	s_nop 0
	ds_read_b128 v[58:61], v236
	ds_read_b128 v[62:65], v236 offset:1024
	ds_read_b128 v[50:53], v236 offset:2048
	ds_read_b128 v[54:57], v236 offset:3072
	ds_read_b128 v[42:45], v236 offset:4096
	ds_read_b128 v[46:49], v236 offset:5120
	ds_read_b128 v[34:37], v236 offset:6144
	ds_read_b128 v[38:41], v236 offset:7168
	global_load_lds_dwordx4 v[68:69], off
	v_lshl_add_u64 v[68:69], s[42:43], 0, v[222:223]
	s_add_i32 m0, s15, 0xe000
	s_nop 0
	global_load_lds_dwordx4 v[68:69], off
	s_cmp_eq_u32 s100, 3
	s_cbranch_scc1 .Lp7vg_w11_a1
	s_cmp_eq_u32 s100, 2
	s_cbranch_scc1 .Lp7vg_wk2_a1
	s_waitcnt vmcnt(8)
	s_branch .Lp7vg_wd_a1

.Lhalfskip_p7a:
	s_cmp_eq_u32 s100, 3
	s_cbranch_scc1 .Lp7dma_w5_a
	s_cmp_eq_u32 s100, 2
	s_cbranch_scc1 .Lp7dma_wk2_a
	s_waitcnt vmcnt(2)
	s_branch .Lp7dma_wd_a
.Lp7dma_wk2_a:
	s_waitcnt vmcnt(4)
	s_branch .Lp7dma_wd_a

.LBB0_790:
	s_barrier
	ds_read_b64_tr_b16 v[26:27], v230 offset:0
	ds_read_b64_tr_b16 v[28:29], v230 offset:1024
	ds_read_b64_tr_b16 v[30:31], v230 offset:8192
	ds_read_b64_tr_b16 v[32:33], v230 offset:9216
	ds_read_b64_tr_b16 v[18:19], v234 offset:0
	ds_read_b64_tr_b16 v[20:21], v234 offset:1024
	ds_read_b64_tr_b16 v[22:23], v234 offset:8192
	ds_read_b64_tr_b16 v[24:25], v234 offset:9216
	ds_read_b64_tr_b16 v[10:11], v231 offset:0
	ds_read_b64_tr_b16 v[12:13], v231 offset:1024
	ds_read_b64_tr_b16 v[14:15], v231 offset:8192
	ds_read_b64_tr_b16 v[16:17], v231 offset:9216
	ds_read_b64_tr_b16 v[2:3], v235 offset:0
	ds_read_b64_tr_b16 v[4:5], v235 offset:1024
	ds_read_b64_tr_b16 v[6:7], v235 offset:8192
	ds_read_b64_tr_b16 v[8:9], v235 offset:9216
	s_add_u32 s4, s4, 0x40000
	s_addc_u32 s5, s5, 0
	s_mov_b32 m0, s50
	v_lshl_add_u64 v[240:241], s[4:5], 0, v[212:213]
	s_nop 0
	ds_read_b128 v[58:61], v236 offset:32768
	ds_read_b128 v[62:65], v236 offset:33792
	ds_read_b128 v[50:53], v236 offset:34816
	ds_read_b128 v[54:57], v236 offset:35840
	ds_read_b128 v[42:45], v236 offset:36864
	ds_read_b128 v[46:49], v236 offset:37888
	ds_read_b128 v[34:37], v236 offset:38912
	ds_read_b128 v[38:41], v236 offset:39936
	global_load_lds_dwordx4 v[240:241], off
	v_lshl_add_u64 v[240:241], s[4:5], 0, v[216:217]
	s_mov_b32 m0, s51
	s_nop 0
	global_load_lds_dwordx4 v[240:241], off
	s_cmp_eq_u32 s100, 3
	s_cbranch_scc1 .Lp7vg_w11_b1
	s_cmp_eq_u32 s100, 2
	s_cbranch_scc1 .Lp7vg_wk2_b1
	s_waitcnt vmcnt(8)
	s_branch .Lp7vg_wd_b1
